# P2 K-loop: expert-weight streamer consume block (scale, fp8 convert, stores) rotated from the loop tail into the next trip's load segment, after the fragment reads are issued
# baseline (speedup 1.0000x reference)
.Lp2_top:
	ds_read_b128 v[158:161], v217
	ds_read_b128 v[162:165], v218
	ds_read_b128 v[166:169], v219
	ds_read_b128 v[170:173], v220
	ds_read_b128 v[148:151], v221
	ds_read_b128 v[144:147], v222
	ds_read_b128 v[140:143], v223
	ds_read_b128 v[136:139], v224
	ds_read_b128 v[174:177], v233
	ds_read_b128 v[178:181], v233 offset:1024
	ds_read_b128 v[182:185], v233 offset:2048
	ds_read_b128 v[186:189], v233 offset:3072
	ds_read_b128 v[190:193], v233 offset:4096
	ds_read_b128 v[194:197], v233 offset:5120
	ds_read_b128 v[234:237], v233 offset:6144
	ds_read_b128 v[238:241], v233 offset:7168
	s_add_i32 s4, s60, s61
	s_mov_b32 s46, s94
	s_add_i32 s94, s94, 1
	s_add_i32 s5, s4, 0x200
	s_add_i32 s16, s33, s61
	s_cmpk_eq_i32 s61, 0x1e00
	s_cselect_b32 s47, s90, s5
	s_cselect_b32 s97, s91, s16
	s_add_i32 s96, s47, 0x80
	s_cmp_eq_u32 s61, 0
	s_cbranch_scc1 .Lp2c_done
	s_bitcmp1_b32 s46, 0
	s_waitcnt vmcnt(15)
	v_mul_f32_e32 v128, 0x42800000, v128
	s_waitcnt vmcnt(14)
	v_mul_f32_e32 v132, 0x42800000, v132
	v_mul_f32_e32 v129, 0x42800000, v129
	v_mul_f32_e32 v133, 0x42800000, v133
	v_mul_f32_e32 v130, 0x42800000, v130
	v_mul_f32_e32 v134, 0x42800000, v134
	v_mul_f32_e32 v131, 0x42800000, v131
	v_mul_f32_e32 v135, 0x42800000, v135
	s_cbranch_scc1 .Lp2c_B
	v_cvt_pk_fp8_f32 v152, v128, v132
	v_cvt_pk_fp8_f32 v153, v129, v133
	v_cvt_pk_fp8_f32 v154, v130, v134
	v_cvt_pk_fp8_f32 v155, v131, v135
	s_branch .Lp2c_done
.Lp2c_B:
	v_cvt_pk_fp8_f32 v152, v128, v132 op_sel:[0,0,1]
	v_cvt_pk_fp8_f32 v153, v129, v133 op_sel:[0,0,1]
	v_cvt_pk_fp8_f32 v154, v130, v134 op_sel:[0,0,1]
	v_cvt_pk_fp8_f32 v155, v131, v135 op_sel:[0,0,1]
	s_cmp_eq_u32 s99, 0
	s_cbranch_scc1 .Lp2c_done
	s_lshl_b32 s98, s67, 10
	s_lshl_b32 s100, s95, 8
	s_or_b32 s98, s98, s100
	s_cmp_lg_u64 s[44:45], 0
	s_cselect_b32 s100, 8, 0
	v_lshlrev_b32_e32 v128, 3, v156
	s_or_b32 s98, s98, s100
	v_and_b32_e32 v128, 0xf0, v128
	v_or_b32_e32 v128, s98, v128
	v_or_b32_e32 v204, v128, v202
	v_lshlrev_b64 v[128:129], 12, v[204:205]
	v_lshl_add_u64 v[128:129], s[6:7], 0, v[128:129]
	s_lshl_b32 s36, s36, 7
	v_lshl_add_u64 v[128:129], v[128:129], 0, s[36:37]
	v_lshl_add_u64 v[128:129], v[128:129], 0, v[200:201]
	s_mov_b32 s100, 0x1000
	s_mov_b32 s101, 0
	global_store_dword v[128:129], v152, off
	v_lshl_add_u64 v[130:131], v[128:129], 0, s[100:101]
	v_lshl_add_u64 v[132:133], v[130:131], 0, s[100:101]
	v_lshl_add_u64 v[134:135], v[132:133], 0, s[100:101]
	global_store_dword v[130:131], v153, off
	global_store_dword v[132:133], v154, off
	global_store_dword v[134:135], v155, off
.Lp2c_done:
	s_mov_b32 m0, s82
	s_add_i32 s5, s4, 0x100180
	buffer_load_dwordx4 v214, s[8:11], s5 offen lds
	s_add_i32 s4, s4, 0x180180
	s_mov_b32 m0, s85
	s_add_i32 vcc_lo, s97, 0x80
	buffer_load_dwordx4 v214, s[8:11], s4 offen lds
	s_lshr_b32 s4, s94, 2
	s_mul_i32 s5, s4, s34
	s_add_i32 s16, s5, s2
	s_cmp_lt_i32 s4, s3
	s_cselect_b64 s[4:5], -1, 0
	s_mov_b32 s99, s4
	s_and_b64 s[44:45], s[4:5], exec
	s_cselect_b32 s16, s16, 0
	s_bfe_u32 s17, s94, 0x10001
	s_or_b32 s17, s17, s83
	s_bfe_u32 s67, s16, 0x50007
	s_bfe_u32 s36, s16, 0x50002
	s_and_b32 s95, s16, 3
	s_cmpk_gt_i32 s16, 0xfff
	s_cselect_b64 s[44:45], -1, 0
	v_lshl_or_b32 v156, s17, 3, v216
	s_and_b64 s[16:17], s[44:45], exec
	s_cselect_b32 s16, s25, s21
	s_cselect_b32 s17, s24, s20
	s_lshl_b32 vcc_hi, s67, 23
	s_add_u32 s17, s17, vcc_hi
	s_addc_u32 s16, s16, 0
	s_lshl_b32 vcc_hi, s36, 18
	s_add_u32 s17, s17, vcc_hi
	s_addc_u32 vcc_hi, s16, 0
	s_lshl_b32 s16, s95, 9
	s_add_u32 s16, s17, s16
	v_and_or_b32 v204, s66, 2, v200
	s_addc_u32 s17, vcc_hi, 0
	v_lshlrev_b64 v[128:129], 11, v[204:205]
	v_lshl_add_u64 v[128:129], s[16:17], 0, v[128:129]
	v_lshlrev_b32_e32 v204, 4, v156
	v_lshl_add_u64 v[132:133], v[128:129], 0, v[204:205]
	global_load_dwordx4 v[128:131], v[132:133], off nt
	s_nop 0
	global_load_dwordx4 v[132:135], v[132:133], off offset:2048 nt
	s_waitcnt vmcnt(10)
	s_waitcnt lgkmcnt(8)
	s_barrier
	s_setprio 1
	s_waitcnt lgkmcnt(7)
	v_mfma_f32_16x16x32_bf16 v[124:127], v[158:161], v[174:177], v[124:127]
	s_waitcnt lgkmcnt(6)
	v_mfma_f32_16x16x32_bf16 v[124:127], v[162:165], v[178:181], v[124:127]
	v_mfma_f32_16x16x32_bf16 v[120:123], v[166:169], v[174:177], v[120:123]
	s_nop 0
	v_mfma_f32_16x16x32_bf16 v[120:123], v[170:173], v[178:181], v[120:123]
	s_waitcnt lgkmcnt(5)
	v_mfma_f32_16x16x32_bf16 v[116:119], v[158:161], v[182:185], v[116:119]
	s_waitcnt lgkmcnt(4)
	v_mfma_f32_16x16x32_bf16 v[116:119], v[162:165], v[186:189], v[116:119]
	v_mfma_f32_16x16x32_bf16 v[112:115], v[166:169], v[182:185], v[112:115]
	s_nop 0
	v_mfma_f32_16x16x32_bf16 v[112:115], v[170:173], v[186:189], v[112:115]
	s_waitcnt lgkmcnt(3)
	v_mfma_f32_16x16x32_bf16 v[108:111], v[158:161], v[190:193], v[108:111]
	s_waitcnt lgkmcnt(2)
	v_mfma_f32_16x16x32_bf16 v[108:111], v[162:165], v[194:197], v[108:111]
	v_mfma_f32_16x16x32_bf16 v[104:107], v[166:169], v[190:193], v[104:107]
	s_nop 0
	v_mfma_f32_16x16x32_bf16 v[104:107], v[170:173], v[194:197], v[104:107]
	s_waitcnt lgkmcnt(1)
	v_mfma_f32_16x16x32_bf16 v[100:103], v[158:161], v[234:237], v[100:103]
	s_waitcnt lgkmcnt(0)
	v_mfma_f32_16x16x32_bf16 v[100:103], v[162:165], v[238:241], v[100:103]
	v_mfma_f32_16x16x32_bf16 v[96:99], v[166:169], v[234:237], v[96:99]
	s_nop 0
	v_mfma_f32_16x16x32_bf16 v[96:99], v[170:173], v[238:241], v[96:99]
	s_setprio 0
	s_setprio 1
	v_mfma_f32_16x16x32_bf16 v[92:95], v[148:151], v[174:177], v[92:95]
	s_nop 0
	v_mfma_f32_16x16x32_bf16 v[92:95], v[144:147], v[178:181], v[92:95]
	v_mfma_f32_16x16x32_bf16 v[88:91], v[140:143], v[174:177], v[88:91]
	s_nop 0
	v_mfma_f32_16x16x32_bf16 v[88:91], v[136:139], v[178:181], v[88:91]
	v_mfma_f32_16x16x32_bf16 v[84:87], v[148:151], v[182:185], v[84:87]
	s_nop 0
	v_mfma_f32_16x16x32_bf16 v[84:87], v[144:147], v[186:189], v[84:87]
	v_mfma_f32_16x16x32_bf16 v[80:83], v[140:143], v[182:185], v[80:83]
	s_nop 0
	v_mfma_f32_16x16x32_bf16 v[80:83], v[136:139], v[186:189], v[80:83]
	v_mfma_f32_16x16x32_bf16 v[76:79], v[148:151], v[190:193], v[76:79]
	s_nop 0
	v_mfma_f32_16x16x32_bf16 v[76:79], v[144:147], v[194:197], v[76:79]
	v_mfma_f32_16x16x32_bf16 v[72:75], v[140:143], v[190:193], v[72:75]
	s_nop 0
	v_mfma_f32_16x16x32_bf16 v[72:75], v[136:139], v[194:197], v[72:75]
	v_mfma_f32_16x16x32_bf16 v[68:71], v[148:151], v[234:237], v[68:71]
	s_nop 0
	v_mfma_f32_16x16x32_bf16 v[68:71], v[144:147], v[238:241], v[68:71]
	v_mfma_f32_16x16x32_bf16 v[64:67], v[140:143], v[234:237], v[64:67]
	s_nop 0
	v_mfma_f32_16x16x32_bf16 v[64:67], v[136:139], v[238:241], v[64:67]
	s_setprio 0
	s_barrier
	ds_read_b128 v[174:177], v233 offset:16384
	ds_read_b128 v[178:181], v233 offset:17408
	ds_read_b128 v[182:185], v233 offset:18432
	ds_read_b128 v[186:189], v233 offset:19456
	ds_read_b128 v[190:193], v233 offset:20480
	ds_read_b128 v[194:197], v233 offset:21504
	ds_read_b128 v[234:237], v233 offset:22528
	ds_read_b128 v[238:241], v233 offset:23552
	s_mov_b32 m0, s65
	s_add_i32 s16, s97, 0x100000
	buffer_load_dwordx4 v215, s[12:15], s97 offen lds
	s_mov_b32 m0, s68
	s_nop 0
	buffer_load_dwordx4 v215, s[12:15], s16 offen lds
	s_add_i32 s16, s97, 0x10000
	s_mov_b32 m0, s69
	s_nop 0
	buffer_load_dwordx4 v215, s[12:15], s16 offen lds
	s_add_i32 s16, s97, 0x110000
	s_mov_b32 m0, s70
	s_nop 0
	buffer_load_dwordx4 v215, s[12:15], s16 offen lds
	s_mov_b32 m0, s64
	s_add_i32 s16, s47, 0x80000
	buffer_load_dwordx4 v214, s[8:11], s47 offen lds
	s_mov_b32 m0, s71
	s_nop 0
	buffer_load_dwordx4 v214, s[8:11], s16 offen lds
	s_waitcnt vmcnt(10)
	s_waitcnt lgkmcnt(6)
	s_barrier
	s_setprio 1
	s_waitcnt lgkmcnt(7)
	v_mfma_f32_16x16x32_bf16 v[60:63], v[158:161], v[174:177], v[60:63]
	s_waitcnt lgkmcnt(6)
	v_mfma_f32_16x16x32_bf16 v[60:63], v[162:165], v[178:181], v[60:63]
	v_mfma_f32_16x16x32_bf16 v[56:59], v[166:169], v[174:177], v[56:59]
	s_nop 0
	v_mfma_f32_16x16x32_bf16 v[56:59], v[170:173], v[178:181], v[56:59]
	s_waitcnt lgkmcnt(5)
	v_mfma_f32_16x16x32_bf16 v[52:55], v[158:161], v[182:185], v[52:55]
	s_waitcnt lgkmcnt(4)
	v_mfma_f32_16x16x32_bf16 v[52:55], v[162:165], v[186:189], v[52:55]
	v_mfma_f32_16x16x32_bf16 v[48:51], v[166:169], v[182:185], v[48:51]
	s_nop 0
	v_mfma_f32_16x16x32_bf16 v[48:51], v[170:173], v[186:189], v[48:51]
	s_waitcnt lgkmcnt(3)
	v_mfma_f32_16x16x32_bf16 v[44:47], v[158:161], v[190:193], v[44:47]
	s_waitcnt lgkmcnt(2)
	v_mfma_f32_16x16x32_bf16 v[44:47], v[162:165], v[194:197], v[44:47]
	v_mfma_f32_16x16x32_bf16 v[40:43], v[166:169], v[190:193], v[40:43]
	s_nop 0
	v_mfma_f32_16x16x32_bf16 v[40:43], v[170:173], v[194:197], v[40:43]
	s_waitcnt lgkmcnt(1)
	v_mfma_f32_16x16x32_bf16 v[36:39], v[158:161], v[234:237], v[36:39]
	s_waitcnt lgkmcnt(0)
	v_mfma_f32_16x16x32_bf16 v[36:39], v[162:165], v[238:241], v[36:39]
	v_mfma_f32_16x16x32_bf16 v[32:35], v[166:169], v[234:237], v[32:35]
	s_nop 0
	v_mfma_f32_16x16x32_bf16 v[32:35], v[170:173], v[238:241], v[32:35]
	s_setprio 0
	s_setprio 1
	v_mfma_f32_16x16x32_bf16 v[28:31], v[148:151], v[174:177], v[28:31]
	s_nop 0
	v_mfma_f32_16x16x32_bf16 v[28:31], v[144:147], v[178:181], v[28:31]
	v_mfma_f32_16x16x32_bf16 v[24:27], v[140:143], v[174:177], v[24:27]
	s_nop 0
	v_mfma_f32_16x16x32_bf16 v[24:27], v[136:139], v[178:181], v[24:27]
	v_mfma_f32_16x16x32_bf16 v[20:23], v[148:151], v[182:185], v[20:23]
	s_nop 0
	v_mfma_f32_16x16x32_bf16 v[20:23], v[144:147], v[186:189], v[20:23]
	v_mfma_f32_16x16x32_bf16 v[16:19], v[140:143], v[182:185], v[16:19]
	s_nop 0
	v_mfma_f32_16x16x32_bf16 v[16:19], v[136:139], v[186:189], v[16:19]
	v_mfma_f32_16x16x32_bf16 v[12:15], v[148:151], v[190:193], v[12:15]
	s_nop 0
	v_mfma_f32_16x16x32_bf16 v[12:15], v[144:147], v[194:197], v[12:15]
	v_mfma_f32_16x16x32_bf16 v[8:11], v[140:143], v[190:193], v[8:11]
	s_nop 0
	v_mfma_f32_16x16x32_bf16 v[8:11], v[136:139], v[194:197], v[8:11]
	v_mfma_f32_16x16x32_bf16 v[4:7], v[148:151], v[234:237], v[4:7]
	s_nop 0
	v_mfma_f32_16x16x32_bf16 v[4:7], v[144:147], v[238:241], v[4:7]
	v_mfma_f32_16x16x32_bf16 v[0:3], v[140:143], v[234:237], v[0:3]
	s_nop 0
	v_mfma_f32_16x16x32_bf16 v[0:3], v[136:139], v[238:241], v[0:3]
	s_setprio 0
	s_barrier
	ds_read_b128 v[136:139], v225
	ds_read_b128 v[140:143], v226
	ds_read_b128 v[144:147], v227
	ds_read_b128 v[148:151], v228
	ds_read_b128 v[158:161], v229
	ds_read_b128 v[162:165], v230
	ds_read_b128 v[166:169], v231
	ds_read_b128 v[170:173], v232
	ds_read_b128 v[174:177], v233 offset:32768
	ds_read_b128 v[178:181], v233 offset:33792
	ds_read_b128 v[182:185], v233 offset:34816
	ds_read_b128 v[186:189], v233 offset:35840
	ds_read_b128 v[190:193], v233 offset:36864
	ds_read_b128 v[194:197], v233 offset:37888
	ds_read_b128 v[234:237], v233 offset:38912
	ds_read_b128 v[238:241], v233 offset:39936
	s_mov_b32 m0, s72
	s_add_i32 s16, s47, 0x100000
	buffer_load_dwordx4 v214, s[8:11], s16 offen lds
	s_add_i32 s16, s47, 0x180000
	s_mov_b32 m0, s73
	s_nop 0
	buffer_load_dwordx4 v214, s[8:11], s16 offen lds
	s_waitcnt vmcnt(10)
	s_waitcnt lgkmcnt(8)
	s_barrier
	s_setprio 1
	s_waitcnt lgkmcnt(7)
	v_mfma_f32_16x16x32_bf16 v[124:127], v[136:139], v[174:177], v[124:127]
	s_waitcnt lgkmcnt(6)
	v_mfma_f32_16x16x32_bf16 v[124:127], v[140:143], v[178:181], v[124:127]
	v_mfma_f32_16x16x32_bf16 v[120:123], v[144:147], v[174:177], v[120:123]
	s_nop 0
	v_mfma_f32_16x16x32_bf16 v[120:123], v[148:151], v[178:181], v[120:123]
	s_waitcnt lgkmcnt(5)
	v_mfma_f32_16x16x32_bf16 v[116:119], v[136:139], v[182:185], v[116:119]
	s_waitcnt lgkmcnt(4)
	v_mfma_f32_16x16x32_bf16 v[116:119], v[140:143], v[186:189], v[116:119]
	v_mfma_f32_16x16x32_bf16 v[112:115], v[144:147], v[182:185], v[112:115]
	s_nop 0
	v_mfma_f32_16x16x32_bf16 v[112:115], v[148:151], v[186:189], v[112:115]
	s_waitcnt lgkmcnt(3)
	v_mfma_f32_16x16x32_bf16 v[108:111], v[136:139], v[190:193], v[108:111]
	s_waitcnt lgkmcnt(2)
	v_mfma_f32_16x16x32_bf16 v[108:111], v[140:143], v[194:197], v[108:111]
	v_mfma_f32_16x16x32_bf16 v[104:107], v[144:147], v[190:193], v[104:107]
	s_nop 0
	v_mfma_f32_16x16x32_bf16 v[104:107], v[148:151], v[194:197], v[104:107]
	s_waitcnt lgkmcnt(1)
	v_mfma_f32_16x16x32_bf16 v[100:103], v[136:139], v[234:237], v[100:103]
	s_waitcnt lgkmcnt(0)
	v_mfma_f32_16x16x32_bf16 v[100:103], v[140:143], v[238:241], v[100:103]
	v_mfma_f32_16x16x32_bf16 v[96:99], v[144:147], v[234:237], v[96:99]
	s_nop 0
	v_mfma_f32_16x16x32_bf16 v[96:99], v[148:151], v[238:241], v[96:99]
	s_setprio 0
	s_setprio 1
	v_mfma_f32_16x16x32_bf16 v[92:95], v[158:161], v[174:177], v[92:95]
	s_nop 0
	v_mfma_f32_16x16x32_bf16 v[92:95], v[162:165], v[178:181], v[92:95]
	v_mfma_f32_16x16x32_bf16 v[88:91], v[166:169], v[174:177], v[88:91]
	s_nop 0
	v_mfma_f32_16x16x32_bf16 v[88:91], v[170:173], v[178:181], v[88:91]
	v_mfma_f32_16x16x32_bf16 v[84:87], v[158:161], v[182:185], v[84:87]
	s_nop 0
	v_mfma_f32_16x16x32_bf16 v[84:87], v[162:165], v[186:189], v[84:87]
	v_mfma_f32_16x16x32_bf16 v[80:83], v[166:169], v[182:185], v[80:83]
	s_nop 0
	v_mfma_f32_16x16x32_bf16 v[80:83], v[170:173], v[186:189], v[80:83]
	v_mfma_f32_16x16x32_bf16 v[76:79], v[158:161], v[190:193], v[76:79]
	s_nop 0
	v_mfma_f32_16x16x32_bf16 v[76:79], v[162:165], v[194:197], v[76:79]
	v_mfma_f32_16x16x32_bf16 v[72:75], v[166:169], v[190:193], v[72:75]
	s_nop 0
	v_mfma_f32_16x16x32_bf16 v[72:75], v[170:173], v[194:197], v[72:75]
	v_mfma_f32_16x16x32_bf16 v[68:71], v[158:161], v[234:237], v[68:71]
	s_nop 0
	v_mfma_f32_16x16x32_bf16 v[68:71], v[162:165], v[238:241], v[68:71]
	v_mfma_f32_16x16x32_bf16 v[64:67], v[166:169], v[234:237], v[64:67]
	s_nop 0
	v_mfma_f32_16x16x32_bf16 v[64:67], v[170:173], v[238:241], v[64:67]
	s_setprio 0
	s_barrier
	ds_read_b128 v[174:177], v233 offset:49152
	ds_read_b128 v[178:181], v233 offset:50176
	ds_read_b128 v[182:185], v233 offset:51200
	ds_read_b128 v[186:189], v233 offset:52224
	ds_read_b128 v[190:193], v233 offset:53248
	ds_read_b128 v[194:197], v233 offset:54272
	ds_read_b128 v[234:237], v233 offset:55296
	ds_read_b128 v[238:241], v233 offset:56320
	s_mov_b32 m0, s76
	s_add_i32 s16, s97, 0x100080
	buffer_load_dwordx4 v215, s[12:15], vcc_lo offen lds
	s_mov_b32 m0, s77
	s_add_i32 s47, s47, 0x80080
	buffer_load_dwordx4 v215, s[12:15], s16 offen lds
	s_add_i32 s16, s97, 0x10080
	s_mov_b32 m0, s80
	s_add_i32 s97, s97, 0x110080
	buffer_load_dwordx4 v215, s[12:15], s16 offen lds
	s_mov_b32 m0, s81
	s_nop 0
	buffer_load_dwordx4 v215, s[12:15], s97 offen lds
	s_mov_b32 m0, s78
	s_nop 0
	buffer_load_dwordx4 v214, s[8:11], s96 offen lds
	s_mov_b32 m0, s79
	s_nop 0
	buffer_load_dwordx4 v214, s[8:11], s47 offen lds
	s_waitcnt vmcnt(8)
	s_waitcnt lgkmcnt(6)
	s_barrier
	s_setprio 1
	s_waitcnt lgkmcnt(7)
	v_mfma_f32_16x16x32_bf16 v[60:63], v[136:139], v[174:177], v[60:63]
	s_waitcnt lgkmcnt(6)
	v_mfma_f32_16x16x32_bf16 v[60:63], v[140:143], v[178:181], v[60:63]
	v_mfma_f32_16x16x32_bf16 v[56:59], v[144:147], v[174:177], v[56:59]
	s_nop 0
	v_mfma_f32_16x16x32_bf16 v[56:59], v[148:151], v[178:181], v[56:59]
	s_waitcnt lgkmcnt(5)
	v_mfma_f32_16x16x32_bf16 v[52:55], v[136:139], v[182:185], v[52:55]
	s_waitcnt lgkmcnt(4)
	v_mfma_f32_16x16x32_bf16 v[52:55], v[140:143], v[186:189], v[52:55]
	v_mfma_f32_16x16x32_bf16 v[48:51], v[144:147], v[182:185], v[48:51]
	s_nop 0
	v_mfma_f32_16x16x32_bf16 v[48:51], v[148:151], v[186:189], v[48:51]
	s_waitcnt lgkmcnt(3)
	v_mfma_f32_16x16x32_bf16 v[44:47], v[136:139], v[190:193], v[44:47]
	s_waitcnt lgkmcnt(2)
	v_mfma_f32_16x16x32_bf16 v[44:47], v[140:143], v[194:197], v[44:47]
	v_mfma_f32_16x16x32_bf16 v[40:43], v[144:147], v[190:193], v[40:43]
	s_nop 0
	v_mfma_f32_16x16x32_bf16 v[40:43], v[148:151], v[194:197], v[40:43]
	s_waitcnt lgkmcnt(1)
	v_mfma_f32_16x16x32_bf16 v[36:39], v[136:139], v[234:237], v[36:39]
	s_waitcnt lgkmcnt(0)
	v_mfma_f32_16x16x32_bf16 v[36:39], v[140:143], v[238:241], v[36:39]
	v_mfma_f32_16x16x32_bf16 v[32:35], v[144:147], v[234:237], v[32:35]
	s_nop 0
	v_mfma_f32_16x16x32_bf16 v[32:35], v[148:151], v[238:241], v[32:35]
	s_setprio 0
	s_setprio 1
	v_mfma_f32_16x16x32_bf16 v[28:31], v[158:161], v[174:177], v[28:31]
	s_nop 0
	v_mfma_f32_16x16x32_bf16 v[28:31], v[162:165], v[178:181], v[28:31]
	v_mfma_f32_16x16x32_bf16 v[24:27], v[166:169], v[174:177], v[24:27]
	s_nop 0
	v_mfma_f32_16x16x32_bf16 v[24:27], v[170:173], v[178:181], v[24:27]
	v_mfma_f32_16x16x32_bf16 v[20:23], v[158:161], v[182:185], v[20:23]
	s_nop 0
	v_mfma_f32_16x16x32_bf16 v[20:23], v[162:165], v[186:189], v[20:23]
	v_mfma_f32_16x16x32_bf16 v[16:19], v[166:169], v[182:185], v[16:19]
	s_nop 0
	v_mfma_f32_16x16x32_bf16 v[16:19], v[170:173], v[186:189], v[16:19]
	v_mfma_f32_16x16x32_bf16 v[12:15], v[158:161], v[190:193], v[12:15]
	s_nop 0
	v_mfma_f32_16x16x32_bf16 v[12:15], v[162:165], v[194:197], v[12:15]
	v_mfma_f32_16x16x32_bf16 v[8:11], v[166:169], v[190:193], v[8:11]
	s_nop 0
	v_mfma_f32_16x16x32_bf16 v[8:11], v[170:173], v[194:197], v[8:11]
	v_mfma_f32_16x16x32_bf16 v[4:7], v[158:161], v[234:237], v[4:7]
	s_nop 0
	v_mfma_f32_16x16x32_bf16 v[4:7], v[162:165], v[238:241], v[4:7]
	v_mfma_f32_16x16x32_bf16 v[0:3], v[166:169], v[234:237], v[0:3]
	s_nop 0
	v_mfma_f32_16x16x32_bf16 v[0:3], v[170:173], v[238:241], v[0:3]
	s_setprio 0
	s_barrier
	s_addk_i32 s61, 0x100
	s_add_i32 s66, s66, 2
	s_cmpk_eq_i32 s61, 0x1f00
	s_cbranch_scc0 .Lp2_top
	s_bitcmp0_b32 s46, 0
	s_waitcnt vmcnt(15)
	v_mul_f32_e32 v128, 0x42800000, v128
	s_waitcnt vmcnt(14)
	v_mul_f32_e32 v132, 0x42800000, v132
	v_mul_f32_e32 v129, 0x42800000, v129
	v_mul_f32_e32 v133, 0x42800000, v133
	v_mul_f32_e32 v130, 0x42800000, v130
	v_mul_f32_e32 v134, 0x42800000, v134
	v_mul_f32_e32 v131, 0x42800000, v131
	v_mul_f32_e32 v135, 0x42800000, v135
	s_mov_b64 s[46:47], -1
	s_cbranch_scc0 .LBB0_350
	s_andn2_b64 vcc, exec, s[46:47]
	s_cbranch_vccnz .LBB0_346
	s_branch .LBB0_351

.LBB0_351:
	v_cvt_pk_fp8_f32 v152, v128, v132 op_sel:[0,0,1]
	v_cvt_pk_fp8_f32 v153, v129, v133 op_sel:[0,0,1]
	v_cvt_pk_fp8_f32 v154, v130, v134 op_sel:[0,0,1]
	v_cvt_pk_fp8_f32 v155, v131, v135 op_sel:[0,0,1]
	s_andn2_b64 vcc, exec, s[4:5]
	s_cbranch_vccnz .LBB0_345
	s_lshl_b32 s4, s67, 10
	s_lshl_b32 s5, s95, 8
	s_or_b32 s16, s4, s5
	s_and_b64 s[4:5], s[44:45], exec
	s_cselect_b32 s4, 8, 0
	v_lshlrev_b32_e32 v128, 3, v156
	s_or_b32 s4, s4, s16
	v_and_b32_e32 v128, 0xf0, v128
	v_or_b32_e32 v128, s4, v128
	v_or_b32_e32 v204, v128, v202
	v_lshlrev_b64 v[128:129], 12, v[204:205]
	v_lshl_add_u64 v[128:129], s[6:7], 0, v[128:129]
	s_lshl_b32 s36, s36, 7
	v_lshl_add_u64 v[128:129], v[128:129], 0, s[36:37]
	v_lshl_add_u64 v[128:129], v[128:129], 0, v[200:201]
	v_add_co_u32_e32 v130, vcc, 0x1000, v128
	global_store_dword v[128:129], v152, off
	s_nop 0
	v_addc_co_u32_e32 v131, vcc, 0, v129, vcc
	global_store_dword v[130:131], v153, off
	v_add_co_u32_e32 v130, vcc, 0x2000, v128
	s_nop 1
	v_addc_co_u32_e32 v131, vcc, 0, v129, vcc
	v_add_co_u32_e32 v128, vcc, 0x3000, v128
	global_store_dword v[130:131], v154, off
	s_nop 0
	v_addc_co_u32_e32 v129, vcc, 0, v129, vcc
	global_store_dword v[128:129], v155, off
	s_branch .LBB0_345
.LBB0_345:
	v_mov_b32_e32 v204, v152
	v_mov_b32_e32 v234, v153
	v_mov_b32_e32 v235, v154
	v_mov_b32_e32 v236, v155
.LBB0_346:
.LBB0_353:
	s_and_b64 vcc, exec, s[38:39]
	s_cbranch_vccz .LBB0_355
	s_barrier
